# P2 rotary-tile epilogue: all 16 cos/sin loads issued together at the epilogue top (were 16 serialized load+vmcnt(0) round trips); P9: unit bias loaded before its K-loop into unused VGPRs, epilogue has
# speedup vs baseline: 1.0018x; 1.0013x over previous
.LBB0_329:
	v_lshl_or_b32 v146, s30, 8, v161
	v_ashrrev_i32_e32 v147, 31, v146
	v_lshl_add_u64 v[28:29], v[146:147], 2, s[22:23]
	global_load_dwordx4 v[40:43], v[28:29], off offset:16
	global_load_dwordx4 v[44:47], v[28:29], off
	global_load_dwordx4 v[24:27], v[28:29], off offset:528
	s_nop 0
	global_load_dwordx4 v[28:31], v[28:29], off offset:512
	s_cmp_gt_i32 s30, 4
	s_cbranch_scc1 .Lp2_rope_pre_done
	s_and_saveexec_b64 vcc, s[26:27]
	v_lshl_add_u32 v244, s33, 8, v160
	v_add_u32_e32 v246, 0x80, v244
	v_ashrrev_i32_e32 v245, 31, v244
	v_ashrrev_i32_e32 v247, 31, v246
	v_lshlrev_b64 v[244:245], 6, v[244:245]
	v_lshlrev_b64 v[246:247], 6, v[246:247]
	v_lshl_add_u64 v[244:245], v[144:145], 0, v[244:245]
	v_lshl_add_u64 v[246:247], v[144:145], 0, v[246:247]
	global_load_dwordx4 v[176:179], v[244:245], off
	global_load_dwordx4 v[180:183], v[244:245], off offset:16
	global_load_dwordx4 v[184:187], v[244:245], off offset:1024
	global_load_dwordx4 v[188:191], v[244:245], off offset:1040
	global_load_dwordx4 v[192:195], v[244:245], off offset:2048
	global_load_dwordx4 v[196:199], v[244:245], off offset:2064
	global_load_dwordx4 v[204:207], v[244:245], off offset:3072
	global_load_dwordx4 v[208:211], v[244:245], off offset:3088
	global_load_dwordx4 v[212:215], v[246:247], off
	global_load_dwordx4 v[216:219], v[246:247], off offset:16
	global_load_dwordx4 v[220:223], v[246:247], off offset:1024
	global_load_dwordx4 v[224:227], v[246:247], off offset:1040
	global_load_dwordx4 v[228:231], v[246:247], off offset:2048
	global_load_dwordx4 v[232:235], v[246:247], off offset:2064
	global_load_dwordx4 v[236:239], v[246:247], off offset:3072
	global_load_dwordx4 v[240:243], v[246:247], off offset:3088
	s_mov_b64 exec, vcc
.Lp2_rope_pre_done:
	s_cmp_lt_i32 s30, 4
	s_cselect_b64 s[18:19], -1, 0
	s_cmp_gt_i32 s30, 3
	s_cselect_b64 s[8:9], -1, 0
	s_add_i32 s4, s30, -13
	s_cmp_lt_u32 s4, 4
	s_cselect_b64 s[4:5], -1, 0
	s_cmp_gt_i32 s30, 4
	s_cselect_b64 s[30:31], -1, 0
	s_mov_b64 s[6:7], -1
	s_and_b64 vcc, exec, s[30:31]
	s_waitcnt vmcnt(3)
	v_pk_add_f32 v[142:143], v[142:143], v[42:43]
	s_waitcnt vmcnt(2)
	v_pk_add_f32 v[148:149], v[138:139], v[46:47]
	v_pk_add_f32 v[138:139], v[136:137], v[44:45]
	v_cndmask_b32_e64 v136, 0, 1, s[4:5]
	v_pk_add_f32 v[140:141], v[140:141], v[40:41]
	v_cmp_ne_u32_e64 s[4:5], 1, v136
	s_cbranch_vccz .LBB0_333
	s_and_b64 vcc, exec, s[4:5]
	v_mov_b32_e32 v167, v143
	v_mov_b32_e32 v166, v142
	v_mov_b32_e32 v164, v141
	v_mov_b32_e32 v152, v140
	v_mov_b32_e32 v169, v149
	v_mov_b32_e32 v168, v148
	v_mov_b32_e32 v165, v139
	v_mov_b32_e32 v153, v138
	s_cbranch_vccnz .LBB0_332
	v_mul_f32_e32 v136, 0xbfb8aa3b, v138
	v_exp_f32_e32 v136, v136
	v_mul_f32_e32 v137, 0xbfb8aa3b, v140
	v_exp_f32_e32 v137, v137
	v_mul_f32_e32 v150, 0xbfb8aa3b, v141
	v_add_f32_e32 v136, 1.0, v136
	v_rcp_f32_e32 v153, v136
	v_mul_f32_e32 v136, 0xbfb8aa3b, v139
	v_exp_f32_e32 v136, v136
	v_exp_f32_e32 v150, v150
	v_add_f32_e32 v137, 1.0, v137
	v_rcp_f32_e32 v152, v137
	v_add_f32_e32 v136, 1.0, v136
	v_mul_f32_e32 v137, 0xbfb8aa3b, v148
	v_rcp_f32_e32 v165, v136
	v_add_f32_e32 v136, 1.0, v150
	v_exp_f32_e32 v137, v137
	v_mul_f32_e32 v150, 0xbfb8aa3b, v142
	v_exp_f32_e32 v150, v150
	v_rcp_f32_e32 v164, v136
	v_add_f32_e32 v136, 1.0, v137
	v_mul_f32_e32 v137, 0xbfb8aa3b, v149
	v_rcp_f32_e32 v168, v136
	v_add_f32_e32 v136, 1.0, v150
	v_exp_f32_e32 v137, v137
	v_mul_f32_e32 v150, 0xbfb8aa3b, v143
	v_exp_f32_e32 v150, v150
	v_rcp_f32_e32 v166, v136
	v_add_f32_e32 v136, 1.0, v137
	v_rcp_f32_e32 v169, v136
	v_add_f32_e32 v136, 1.0, v150
	v_rcp_f32_e32 v167, v136

.LBB0_333:
	v_lshl_add_u32 v136, s33, 8, v160
	v_ashrrev_i32_e32 v137, 31, v136
	s_andn2_b64 vcc, exec, s[6:7]
	v_lshlrev_b64 v[150:151], 6, v[136:137]
	s_cbranch_vccnz .LBB0_339
	s_and_saveexec_b64 s[6:7], s[26:27]
	s_cbranch_execz .LBB0_336
	s_waitcnt vmcnt(0)
	v_lshl_add_u64 v[152:153], v[144:145], 0, v[150:151]
	v_mov_b64_e32 v[164:165], v[180:181]
	v_mov_b64_e32 v[166:167], v[182:183]
	v_mov_b64_e32 v[168:169], v[176:177]
	v_mov_b64_e32 v[170:171], v[178:179]
	v_pk_mul_f32 v[174:175], v[140:141], v[164:165] op_sel:[1,1] op_sel_hi:[0,1]
	v_pk_mul_f32 v[172:173], v[138:139], v[168:169] op_sel:[1,1] op_sel_hi:[0,1]
	v_pk_mul_f32 v[152:153], v[138:139], v[168:169]
	v_pk_fma_f32 v[138:139], v[138:139], v[168:169], v[172:173] op_sel_hi:[1,0,1]
	s_nop 0
	v_mul_f32_e32 v138, v149, v171
	v_pk_fma_f32 v[168:169], v[148:149], v[170:171], v[138:139] op_sel_hi:[1,1,0] neg_lo:[0,0,1] neg_hi:[0,0,1]
	v_mul_f32_e32 v138, v148, v171
	v_pk_fma_f32 v[170:171], v[148:149], v[170:171], v[138:139] op_sel:[1,0,0] op_sel_hi:[0,1,0]
	v_mul_f32_e32 v138, v143, v167
	v_pk_mul_f32 v[148:149], v[140:141], v[164:165]
	v_pk_fma_f32 v[140:141], v[140:141], v[164:165], v[174:175] op_sel_hi:[1,0,1]
	v_pk_fma_f32 v[164:165], v[142:143], v[166:167], v[138:139] op_sel_hi:[1,1,0] neg_lo:[0,0,1] neg_hi:[0,0,1]
	v_mul_f32_e32 v138, v142, v167
	v_pk_fma_f32 v[166:167], v[142:143], v[166:167], v[138:139] op_sel:[1,0,0] op_sel_hi:[0,1,0]
	v_sub_f32_e32 v138, v152, v172
	v_sub_f32_e32 v140, v148, v174
	v_mov_b32_e32 v148, v168
	v_mov_b32_e32 v149, v170
	v_mov_b32_e32 v142, v164
	v_mov_b32_e32 v143, v166

.LBB0_343:
	s_andn2_b64 vcc, exec, s[8:9]
	s_cbranch_vccnz .LBB0_347
	s_and_saveexec_b64 s[8:9], s[26:27]
	s_cbranch_execz .LBB0_346
	v_lshl_add_u64 v[148:149], v[144:145], 0, v[150:151]
	v_mov_b64_e32 v[140:141], v[180:181]
	v_mov_b64_e32 v[142:143], v[182:183]
	v_mov_b64_e32 v[148:149], v[176:177]
	v_mov_b64_e32 v[150:151], v[178:179]
	v_pk_mul_f32 v[166:167], v[128:129], v[140:141] op_sel:[1,1] op_sel_hi:[0,1]
	v_pk_mul_f32 v[164:165], v[132:133], v[148:149] op_sel:[1,1] op_sel_hi:[0,1]
	v_pk_mul_f32 v[152:153], v[132:133], v[148:149]
	v_pk_fma_f32 v[132:133], v[132:133], v[148:149], v[164:165] op_sel_hi:[1,0,1]
	s_nop 0
	v_mul_f32_e32 v132, v135, v151
	v_pk_fma_f32 v[148:149], v[134:135], v[150:151], v[132:133] op_sel_hi:[1,1,0] neg_lo:[0,0,1] neg_hi:[0,0,1]
	v_mul_f32_e32 v132, v134, v151
	v_pk_fma_f32 v[150:151], v[134:135], v[150:151], v[132:133] op_sel:[1,0,0] op_sel_hi:[0,1,0]
	v_pk_mul_f32 v[134:135], v[128:129], v[140:141]
	v_pk_fma_f32 v[128:129], v[128:129], v[140:141], v[166:167] op_sel_hi:[1,0,1]
	v_sub_f32_e32 v132, v152, v164
	v_mul_f32_e32 v128, v131, v143
	v_pk_fma_f32 v[140:141], v[130:131], v[142:143], v[128:129] op_sel_hi:[1,1,0] neg_lo:[0,0,1] neg_hi:[0,0,1]
	v_mul_f32_e32 v128, v130, v143
	v_pk_fma_f32 v[142:143], v[130:131], v[142:143], v[128:129] op_sel:[1,0,0] op_sel_hi:[0,1,0]
	v_sub_f32_e32 v128, v134, v166
	v_mov_b32_e32 v134, v148
	v_mov_b32_e32 v135, v150
	v_mov_b32_e32 v130, v140
	v_mov_b32_e32 v131, v142

.LBB0_351:
	v_or_b32_e32 v130, 16, v136
	v_ashrrev_i32_e32 v131, 31, v130
	s_andn2_b64 vcc, exec, s[30:31]
	v_lshlrev_b64 v[120:121], 6, v[130:131]
	s_cbranch_vccnz .LBB0_357
	s_and_saveexec_b64 s[30:31], s[26:27]
	s_cbranch_execz .LBB0_354
	v_lshl_add_u64 v[138:139], v[144:145], 0, v[120:121]
	v_mov_b64_e32 v[132:133], v[188:189]
	v_mov_b64_e32 v[134:135], v[190:191]
	v_mov_b64_e32 v[138:139], v[184:185]
	v_mov_b64_e32 v[140:141], v[186:187]
	v_pk_mul_f32 v[150:151], v[122:123], v[132:133] op_sel:[1,1] op_sel_hi:[0,1]
	v_pk_mul_f32 v[148:149], v[124:125], v[138:139] op_sel:[1,1] op_sel_hi:[0,1]
	v_pk_mul_f32 v[142:143], v[124:125], v[138:139]
	v_pk_fma_f32 v[124:125], v[124:125], v[138:139], v[148:149] op_sel_hi:[1,0,1]
	s_nop 0
	v_mul_f32_e32 v124, v129, v141
	v_pk_fma_f32 v[138:139], v[128:129], v[140:141], v[124:125] op_sel_hi:[1,1,0] neg_lo:[0,0,1] neg_hi:[0,0,1]
	v_mul_f32_e32 v124, v128, v141
	v_pk_fma_f32 v[140:141], v[128:129], v[140:141], v[124:125] op_sel:[1,0,0] op_sel_hi:[0,1,0]
	v_pk_mul_f32 v[128:129], v[122:123], v[132:133]
	v_pk_fma_f32 v[122:123], v[122:123], v[132:133], v[150:151] op_sel_hi:[1,0,1]
	v_sub_f32_e32 v124, v142, v148
	v_mul_f32_e32 v122, v127, v135
	v_pk_fma_f32 v[132:133], v[126:127], v[134:135], v[122:123] op_sel_hi:[1,1,0] neg_lo:[0,0,1] neg_hi:[0,0,1]
	v_mul_f32_e32 v122, v126, v135
	v_pk_fma_f32 v[134:135], v[126:127], v[134:135], v[122:123] op_sel:[1,0,0] op_sel_hi:[0,1,0]
	v_sub_f32_e32 v122, v128, v150
	v_mov_b32_e32 v128, v138
	v_mov_b32_e32 v129, v140
	v_mov_b32_e32 v126, v132
	v_mov_b32_e32 v127, v134

.LBB0_361:
	s_andn2_b64 vcc, exec, s[30:31]
	s_cbranch_vccnz .LBB0_365
	s_and_saveexec_b64 s[30:31], s[26:27]
	s_cbranch_execz .LBB0_364
	v_lshl_add_u64 v[120:121], v[144:145], 0, v[120:121]
	v_mov_b64_e32 v[124:125], v[188:189]
	v_mov_b64_e32 v[126:127], v[190:191]
	v_mov_b64_e32 v[128:129], v[184:185]
	v_mov_b64_e32 v[130:131], v[186:187]
	v_pk_mul_f32 v[134:135], v[112:113], v[124:125] op_sel:[1,1] op_sel_hi:[0,1]
	v_pk_mul_f32 v[132:133], v[116:117], v[128:129] op_sel:[1,1] op_sel_hi:[0,1]
	v_pk_mul_f32 v[120:121], v[116:117], v[128:129]
	v_pk_fma_f32 v[116:117], v[116:117], v[128:129], v[132:133] op_sel_hi:[1,0,1]
	s_nop 0
	v_mul_f32_e32 v116, v119, v131
	v_pk_fma_f32 v[128:129], v[118:119], v[130:131], v[116:117] op_sel_hi:[1,1,0] neg_lo:[0,0,1] neg_hi:[0,0,1]
	v_mul_f32_e32 v116, v118, v131
	v_pk_fma_f32 v[130:131], v[118:119], v[130:131], v[116:117] op_sel:[1,0,0] op_sel_hi:[0,1,0]
	v_pk_mul_f32 v[118:119], v[112:113], v[124:125]
	v_pk_fma_f32 v[112:113], v[112:113], v[124:125], v[134:135] op_sel_hi:[1,0,1]
	v_sub_f32_e32 v116, v120, v132
	v_mul_f32_e32 v112, v115, v127
	v_pk_fma_f32 v[124:125], v[114:115], v[126:127], v[112:113] op_sel_hi:[1,1,0] neg_lo:[0,0,1] neg_hi:[0,0,1]
	v_mul_f32_e32 v112, v114, v127
	v_pk_fma_f32 v[126:127], v[114:115], v[126:127], v[112:113] op_sel:[1,0,0] op_sel_hi:[0,1,0]
	v_sub_f32_e32 v112, v118, v134
	v_mov_b32_e32 v118, v128
	v_mov_b32_e32 v119, v130
	v_mov_b32_e32 v114, v124
	v_mov_b32_e32 v115, v126

.LBB0_369:
	v_or_b32_e32 v114, 32, v136
	v_ashrrev_i32_e32 v115, 31, v114
	s_andn2_b64 vcc, exec, s[30:31]
	v_lshlrev_b64 v[104:105], 6, v[114:115]
	s_cbranch_vccnz .LBB0_375
	s_and_saveexec_b64 s[30:31], s[26:27]
	s_cbranch_execz .LBB0_372
	v_lshl_add_u64 v[120:121], v[144:145], 0, v[104:105]
	v_mov_b64_e32 v[116:117], v[196:197]
	v_mov_b64_e32 v[118:119], v[198:199]
	v_mov_b64_e32 v[120:121], v[192:193]
	v_mov_b64_e32 v[122:123], v[194:195]
	v_pk_mul_f32 v[128:129], v[106:107], v[116:117] op_sel:[1,1] op_sel_hi:[0,1]
	v_pk_mul_f32 v[126:127], v[108:109], v[120:121] op_sel:[1,1] op_sel_hi:[0,1]
	v_pk_mul_f32 v[124:125], v[108:109], v[120:121]
	v_pk_fma_f32 v[108:109], v[108:109], v[120:121], v[126:127] op_sel_hi:[1,0,1]
	s_nop 0
	v_mul_f32_e32 v108, v113, v123
	v_pk_fma_f32 v[120:121], v[112:113], v[122:123], v[108:109] op_sel_hi:[1,1,0] neg_lo:[0,0,1] neg_hi:[0,0,1]
	v_mul_f32_e32 v108, v112, v123
	v_pk_fma_f32 v[122:123], v[112:113], v[122:123], v[108:109] op_sel:[1,0,0] op_sel_hi:[0,1,0]
	v_pk_mul_f32 v[112:113], v[106:107], v[116:117]
	v_pk_fma_f32 v[106:107], v[106:107], v[116:117], v[128:129] op_sel_hi:[1,0,1]
	v_sub_f32_e32 v108, v124, v126
	v_mul_f32_e32 v106, v111, v119
	v_pk_fma_f32 v[116:117], v[110:111], v[118:119], v[106:107] op_sel_hi:[1,1,0] neg_lo:[0,0,1] neg_hi:[0,0,1]
	v_mul_f32_e32 v106, v110, v119
	v_pk_fma_f32 v[118:119], v[110:111], v[118:119], v[106:107] op_sel:[1,0,0] op_sel_hi:[0,1,0]
	v_sub_f32_e32 v106, v112, v128
	v_mov_b32_e32 v112, v120
	v_mov_b32_e32 v113, v122
	v_mov_b32_e32 v110, v116
	v_mov_b32_e32 v111, v118

.LBB0_379:
	s_andn2_b64 vcc, exec, s[30:31]
	s_cbranch_vccnz .LBB0_383
	s_and_saveexec_b64 s[30:31], s[26:27]
	s_cbranch_execz .LBB0_382
	v_lshl_add_u64 v[104:105], v[144:145], 0, v[104:105]
	v_mov_b64_e32 v[108:109], v[196:197]
	v_mov_b64_e32 v[110:111], v[198:199]
	v_mov_b64_e32 v[112:113], v[192:193]
	v_mov_b64_e32 v[114:115], v[194:195]
	v_pk_mul_f32 v[118:119], v[96:97], v[108:109] op_sel:[1,1] op_sel_hi:[0,1]
	v_pk_mul_f32 v[116:117], v[100:101], v[112:113] op_sel:[1,1] op_sel_hi:[0,1]
	v_pk_mul_f32 v[104:105], v[100:101], v[112:113]
	v_pk_fma_f32 v[100:101], v[100:101], v[112:113], v[116:117] op_sel_hi:[1,0,1]
	s_nop 0
	v_mul_f32_e32 v100, v103, v115
	v_pk_fma_f32 v[112:113], v[102:103], v[114:115], v[100:101] op_sel_hi:[1,1,0] neg_lo:[0,0,1] neg_hi:[0,0,1]
	v_mul_f32_e32 v100, v102, v115
	v_pk_fma_f32 v[114:115], v[102:103], v[114:115], v[100:101] op_sel:[1,0,0] op_sel_hi:[0,1,0]
	v_pk_mul_f32 v[102:103], v[96:97], v[108:109]
	v_pk_fma_f32 v[96:97], v[96:97], v[108:109], v[118:119] op_sel_hi:[1,0,1]
	v_sub_f32_e32 v100, v104, v116
	v_mul_f32_e32 v96, v99, v111
	v_pk_fma_f32 v[108:109], v[98:99], v[110:111], v[96:97] op_sel_hi:[1,1,0] neg_lo:[0,0,1] neg_hi:[0,0,1]
	v_mul_f32_e32 v96, v98, v111
	v_pk_fma_f32 v[110:111], v[98:99], v[110:111], v[96:97] op_sel:[1,0,0] op_sel_hi:[0,1,0]
	v_sub_f32_e32 v96, v102, v118
	v_mov_b32_e32 v102, v112
	v_mov_b32_e32 v103, v114
	v_mov_b32_e32 v98, v108
	v_mov_b32_e32 v99, v110

.LBB0_387:
	v_or_b32_e32 v98, 48, v136
	v_ashrrev_i32_e32 v99, 31, v98
	s_andn2_b64 vcc, exec, s[30:31]
	v_lshlrev_b64 v[88:89], 6, v[98:99]
	s_cbranch_vccnz .LBB0_393
	s_and_saveexec_b64 s[30:31], s[26:27]
	s_cbranch_execz .LBB0_390
	v_lshl_add_u64 v[104:105], v[144:145], 0, v[88:89]
	v_mov_b64_e32 v[100:101], v[208:209]
	v_mov_b64_e32 v[102:103], v[210:211]
	v_mov_b64_e32 v[104:105], v[204:205]
	v_mov_b64_e32 v[106:107], v[206:207]
	v_pk_mul_f32 v[112:113], v[90:91], v[100:101] op_sel:[1,1] op_sel_hi:[0,1]
	v_pk_mul_f32 v[110:111], v[92:93], v[104:105] op_sel:[1,1] op_sel_hi:[0,1]
	v_pk_mul_f32 v[108:109], v[92:93], v[104:105]
	v_pk_fma_f32 v[92:93], v[92:93], v[104:105], v[110:111] op_sel_hi:[1,0,1]
	s_nop 0
	v_mul_f32_e32 v92, v97, v107
	v_pk_fma_f32 v[104:105], v[96:97], v[106:107], v[92:93] op_sel_hi:[1,1,0] neg_lo:[0,0,1] neg_hi:[0,0,1]
	v_mul_f32_e32 v92, v96, v107
	v_pk_fma_f32 v[106:107], v[96:97], v[106:107], v[92:93] op_sel:[1,0,0] op_sel_hi:[0,1,0]
	v_pk_mul_f32 v[96:97], v[90:91], v[100:101]
	v_pk_fma_f32 v[90:91], v[90:91], v[100:101], v[112:113] op_sel_hi:[1,0,1]
	v_sub_f32_e32 v92, v108, v110
	v_mul_f32_e32 v90, v95, v103
	v_pk_fma_f32 v[100:101], v[94:95], v[102:103], v[90:91] op_sel_hi:[1,1,0] neg_lo:[0,0,1] neg_hi:[0,0,1]
	v_mul_f32_e32 v90, v94, v103
	v_pk_fma_f32 v[102:103], v[94:95], v[102:103], v[90:91] op_sel:[1,0,0] op_sel_hi:[0,1,0]
	v_sub_f32_e32 v90, v96, v112
	v_mov_b32_e32 v96, v104
	v_mov_b32_e32 v97, v106
	v_mov_b32_e32 v94, v100
	v_mov_b32_e32 v95, v102

.LBB0_397:
	s_andn2_b64 vcc, exec, s[30:31]
	s_cbranch_vccnz .LBB0_401
	s_and_saveexec_b64 s[30:31], s[26:27]
	s_cbranch_execz .LBB0_400
	v_lshl_add_u64 v[88:89], v[144:145], 0, v[88:89]
	v_mov_b64_e32 v[92:93], v[208:209]
	v_mov_b64_e32 v[94:95], v[210:211]
	v_mov_b64_e32 v[96:97], v[204:205]
	v_mov_b64_e32 v[98:99], v[206:207]
	v_pk_mul_f32 v[102:103], v[80:81], v[92:93] op_sel:[1,1] op_sel_hi:[0,1]
	v_pk_mul_f32 v[100:101], v[84:85], v[96:97] op_sel:[1,1] op_sel_hi:[0,1]
	v_pk_mul_f32 v[88:89], v[84:85], v[96:97]
	v_pk_fma_f32 v[84:85], v[84:85], v[96:97], v[100:101] op_sel_hi:[1,0,1]
	s_nop 0
	v_mul_f32_e32 v84, v87, v99
	v_pk_fma_f32 v[96:97], v[86:87], v[98:99], v[84:85] op_sel_hi:[1,1,0] neg_lo:[0,0,1] neg_hi:[0,0,1]
	v_mul_f32_e32 v84, v86, v99
	v_pk_fma_f32 v[98:99], v[86:87], v[98:99], v[84:85] op_sel:[1,0,0] op_sel_hi:[0,1,0]
	v_pk_mul_f32 v[86:87], v[80:81], v[92:93]
	v_pk_fma_f32 v[80:81], v[80:81], v[92:93], v[102:103] op_sel_hi:[1,0,1]
	v_sub_f32_e32 v84, v88, v100
	v_mul_f32_e32 v80, v83, v95
	v_pk_fma_f32 v[92:93], v[82:83], v[94:95], v[80:81] op_sel_hi:[1,1,0] neg_lo:[0,0,1] neg_hi:[0,0,1]
	v_mul_f32_e32 v80, v82, v95
	v_pk_fma_f32 v[94:95], v[82:83], v[94:95], v[80:81] op_sel:[1,0,0] op_sel_hi:[0,1,0]
	v_sub_f32_e32 v80, v86, v102
	v_mov_b32_e32 v86, v96
	v_mov_b32_e32 v87, v98
	v_mov_b32_e32 v82, v92
	v_mov_b32_e32 v83, v94

.LBB0_405:
	v_add_u32_e32 v82, 0x80, v136
	v_ashrrev_i32_e32 v83, 31, v82
	s_andn2_b64 vcc, exec, s[30:31]
	v_lshlrev_b64 v[72:73], 6, v[82:83]
	s_cbranch_vccnz .LBB0_411
	s_and_saveexec_b64 s[30:31], s[26:27]
	s_cbranch_execz .LBB0_408
	v_lshl_add_u64 v[88:89], v[144:145], 0, v[72:73]
	v_mov_b64_e32 v[84:85], v[216:217]
	v_mov_b64_e32 v[86:87], v[218:219]
	v_mov_b64_e32 v[88:89], v[212:213]
	v_mov_b64_e32 v[90:91], v[214:215]
	v_pk_mul_f32 v[96:97], v[74:75], v[84:85] op_sel:[1,1] op_sel_hi:[0,1]
	v_pk_mul_f32 v[94:95], v[76:77], v[88:89] op_sel:[1,1] op_sel_hi:[0,1]
	v_pk_mul_f32 v[92:93], v[76:77], v[88:89]
	v_pk_fma_f32 v[76:77], v[76:77], v[88:89], v[94:95] op_sel_hi:[1,0,1]
	s_nop 0
	v_mul_f32_e32 v76, v81, v91
	v_pk_fma_f32 v[88:89], v[80:81], v[90:91], v[76:77] op_sel_hi:[1,1,0] neg_lo:[0,0,1] neg_hi:[0,0,1]
	v_mul_f32_e32 v76, v80, v91
	v_pk_fma_f32 v[90:91], v[80:81], v[90:91], v[76:77] op_sel:[1,0,0] op_sel_hi:[0,1,0]
	v_pk_mul_f32 v[80:81], v[74:75], v[84:85]
	v_pk_fma_f32 v[74:75], v[74:75], v[84:85], v[96:97] op_sel_hi:[1,0,1]
	v_sub_f32_e32 v76, v92, v94
	v_mul_f32_e32 v74, v79, v87
	v_pk_fma_f32 v[84:85], v[78:79], v[86:87], v[74:75] op_sel_hi:[1,1,0] neg_lo:[0,0,1] neg_hi:[0,0,1]
	v_mul_f32_e32 v74, v78, v87
	v_pk_fma_f32 v[86:87], v[78:79], v[86:87], v[74:75] op_sel:[1,0,0] op_sel_hi:[0,1,0]
	v_sub_f32_e32 v74, v80, v96
	v_mov_b32_e32 v80, v88
	v_mov_b32_e32 v81, v90
	v_mov_b32_e32 v78, v84
	v_mov_b32_e32 v79, v86

.LBB0_415:
	s_andn2_b64 vcc, exec, s[30:31]
	s_cbranch_vccnz .LBB0_419
	s_and_saveexec_b64 s[30:31], s[26:27]
	s_cbranch_execz .LBB0_418
	v_lshl_add_u64 v[72:73], v[144:145], 0, v[72:73]
	v_mov_b64_e32 v[76:77], v[216:217]
	v_mov_b64_e32 v[78:79], v[218:219]
	v_mov_b64_e32 v[80:81], v[212:213]
	v_mov_b64_e32 v[82:83], v[214:215]
	v_pk_mul_f32 v[86:87], v[64:65], v[76:77] op_sel:[1,1] op_sel_hi:[0,1]
	v_pk_mul_f32 v[84:85], v[68:69], v[80:81] op_sel:[1,1] op_sel_hi:[0,1]
	v_pk_mul_f32 v[72:73], v[68:69], v[80:81]
	v_pk_fma_f32 v[68:69], v[68:69], v[80:81], v[84:85] op_sel_hi:[1,0,1]
	s_nop 0
	v_mul_f32_e32 v68, v71, v83
	v_pk_fma_f32 v[80:81], v[70:71], v[82:83], v[68:69] op_sel_hi:[1,1,0] neg_lo:[0,0,1] neg_hi:[0,0,1]
	v_mul_f32_e32 v68, v70, v83
	v_pk_fma_f32 v[82:83], v[70:71], v[82:83], v[68:69] op_sel:[1,0,0] op_sel_hi:[0,1,0]
	v_pk_mul_f32 v[70:71], v[64:65], v[76:77]
	v_pk_fma_f32 v[64:65], v[64:65], v[76:77], v[86:87] op_sel_hi:[1,0,1]
	v_sub_f32_e32 v68, v72, v84
	v_mul_f32_e32 v64, v67, v79
	v_pk_fma_f32 v[76:77], v[66:67], v[78:79], v[64:65] op_sel_hi:[1,1,0] neg_lo:[0,0,1] neg_hi:[0,0,1]
	v_mul_f32_e32 v64, v66, v79
	v_pk_fma_f32 v[78:79], v[66:67], v[78:79], v[64:65] op_sel:[1,0,0] op_sel_hi:[0,1,0]
	v_sub_f32_e32 v64, v70, v86
	v_mov_b32_e32 v70, v80
	v_mov_b32_e32 v71, v82
	v_mov_b32_e32 v66, v76
	v_mov_b32_e32 v67, v78

.LBB0_423:
	v_add_u32_e32 v66, 0x90, v136
	v_ashrrev_i32_e32 v67, 31, v66
	s_andn2_b64 vcc, exec, s[30:31]
	v_lshlrev_b64 v[56:57], 6, v[66:67]
	s_cbranch_vccnz .LBB0_429
	s_and_saveexec_b64 s[30:31], s[26:27]
	s_cbranch_execz .LBB0_426
	v_lshl_add_u64 v[72:73], v[144:145], 0, v[56:57]
	v_mov_b64_e32 v[68:69], v[224:225]
	v_mov_b64_e32 v[70:71], v[226:227]
	v_mov_b64_e32 v[72:73], v[220:221]
	v_mov_b64_e32 v[74:75], v[222:223]
	v_pk_mul_f32 v[80:81], v[58:59], v[68:69] op_sel:[1,1] op_sel_hi:[0,1]
	v_pk_mul_f32 v[78:79], v[60:61], v[72:73] op_sel:[1,1] op_sel_hi:[0,1]
	v_pk_mul_f32 v[76:77], v[60:61], v[72:73]
	v_pk_fma_f32 v[60:61], v[60:61], v[72:73], v[78:79] op_sel_hi:[1,0,1]
	s_nop 0
	v_mul_f32_e32 v60, v65, v75
	v_pk_fma_f32 v[72:73], v[64:65], v[74:75], v[60:61] op_sel_hi:[1,1,0] neg_lo:[0,0,1] neg_hi:[0,0,1]
	v_mul_f32_e32 v60, v64, v75
	v_pk_fma_f32 v[74:75], v[64:65], v[74:75], v[60:61] op_sel:[1,0,0] op_sel_hi:[0,1,0]
	v_pk_mul_f32 v[64:65], v[58:59], v[68:69]
	v_pk_fma_f32 v[58:59], v[58:59], v[68:69], v[80:81] op_sel_hi:[1,0,1]
	v_sub_f32_e32 v60, v76, v78
	v_mul_f32_e32 v58, v63, v71
	v_pk_fma_f32 v[68:69], v[62:63], v[70:71], v[58:59] op_sel_hi:[1,1,0] neg_lo:[0,0,1] neg_hi:[0,0,1]
	v_mul_f32_e32 v58, v62, v71
	v_pk_fma_f32 v[70:71], v[62:63], v[70:71], v[58:59] op_sel:[1,0,0] op_sel_hi:[0,1,0]
	v_sub_f32_e32 v58, v64, v80
	v_mov_b32_e32 v64, v72
	v_mov_b32_e32 v65, v74
	v_mov_b32_e32 v62, v68
	v_mov_b32_e32 v63, v70

.LBB0_433:
	s_andn2_b64 vcc, exec, s[30:31]
	s_cbranch_vccnz .LBB0_437
	s_and_saveexec_b64 s[30:31], s[26:27]
	s_cbranch_execz .LBB0_436
	v_lshl_add_u64 v[56:57], v[144:145], 0, v[56:57]
	v_mov_b64_e32 v[60:61], v[224:225]
	v_mov_b64_e32 v[62:63], v[226:227]
	v_mov_b64_e32 v[64:65], v[220:221]
	v_mov_b64_e32 v[66:67], v[222:223]
	v_pk_mul_f32 v[70:71], v[48:49], v[60:61] op_sel:[1,1] op_sel_hi:[0,1]
	v_pk_mul_f32 v[68:69], v[52:53], v[64:65] op_sel:[1,1] op_sel_hi:[0,1]
	v_pk_mul_f32 v[56:57], v[52:53], v[64:65]
	v_pk_fma_f32 v[52:53], v[52:53], v[64:65], v[68:69] op_sel_hi:[1,0,1]
	s_nop 0
	v_mul_f32_e32 v52, v55, v67
	v_pk_fma_f32 v[64:65], v[54:55], v[66:67], v[52:53] op_sel_hi:[1,1,0] neg_lo:[0,0,1] neg_hi:[0,0,1]
	v_mul_f32_e32 v52, v54, v67
	v_pk_fma_f32 v[66:67], v[54:55], v[66:67], v[52:53] op_sel:[1,0,0] op_sel_hi:[0,1,0]
	v_pk_mul_f32 v[54:55], v[48:49], v[60:61]
	v_pk_fma_f32 v[48:49], v[48:49], v[60:61], v[70:71] op_sel_hi:[1,0,1]
	v_sub_f32_e32 v52, v56, v68
	v_mul_f32_e32 v48, v51, v63
	v_pk_fma_f32 v[60:61], v[50:51], v[62:63], v[48:49] op_sel_hi:[1,1,0] neg_lo:[0,0,1] neg_hi:[0,0,1]
	v_mul_f32_e32 v48, v50, v63
	v_pk_fma_f32 v[62:63], v[50:51], v[62:63], v[48:49] op_sel:[1,0,0] op_sel_hi:[0,1,0]
	v_sub_f32_e32 v48, v54, v70
	v_mov_b32_e32 v54, v64
	v_mov_b32_e32 v55, v66
	v_mov_b32_e32 v50, v60
	v_mov_b32_e32 v51, v62

.LBB0_441:
	v_add_u32_e32 v50, 0xa0, v136
	v_ashrrev_i32_e32 v51, 31, v50
	s_andn2_b64 vcc, exec, s[30:31]
	v_lshlrev_b64 v[32:33], 6, v[50:51]
	s_cbranch_vccnz .LBB0_447
	s_and_saveexec_b64 s[30:31], s[26:27]
	s_cbranch_execz .LBB0_444
	v_lshl_add_u64 v[56:57], v[144:145], 0, v[32:33]
	v_mov_b64_e32 v[52:53], v[232:233]
	v_mov_b64_e32 v[54:55], v[234:235]
	v_mov_b64_e32 v[56:57], v[228:229]
	v_mov_b64_e32 v[58:59], v[230:231]
	v_pk_mul_f32 v[64:65], v[34:35], v[52:53] op_sel:[1,1] op_sel_hi:[0,1]
	v_pk_mul_f32 v[62:63], v[36:37], v[56:57] op_sel:[1,1] op_sel_hi:[0,1]
	v_pk_mul_f32 v[60:61], v[36:37], v[56:57]
	v_pk_fma_f32 v[36:37], v[36:37], v[56:57], v[62:63] op_sel_hi:[1,0,1]
	s_nop 0
	v_mul_f32_e32 v36, v49, v59
	v_pk_fma_f32 v[56:57], v[48:49], v[58:59], v[36:37] op_sel_hi:[1,1,0] neg_lo:[0,0,1] neg_hi:[0,0,1]
	v_mul_f32_e32 v36, v48, v59
	v_pk_fma_f32 v[58:59], v[48:49], v[58:59], v[36:37] op_sel:[1,0,0] op_sel_hi:[0,1,0]
	v_pk_mul_f32 v[48:49], v[34:35], v[52:53]
	v_pk_fma_f32 v[34:35], v[34:35], v[52:53], v[64:65] op_sel_hi:[1,0,1]
	v_sub_f32_e32 v36, v60, v62
	v_mul_f32_e32 v34, v39, v55
	v_pk_fma_f32 v[52:53], v[38:39], v[54:55], v[34:35] op_sel_hi:[1,1,0] neg_lo:[0,0,1] neg_hi:[0,0,1]
	v_mul_f32_e32 v34, v38, v55
	v_pk_fma_f32 v[54:55], v[38:39], v[54:55], v[34:35] op_sel:[1,0,0] op_sel_hi:[0,1,0]
	v_sub_f32_e32 v34, v48, v64
	v_mov_b32_e32 v48, v56
	v_mov_b32_e32 v49, v58
	v_mov_b32_e32 v38, v52
	v_mov_b32_e32 v39, v54

.LBB0_451:
	s_andn2_b64 vcc, exec, s[30:31]
	s_cbranch_vccnz .LBB0_455
	s_and_saveexec_b64 s[30:31], s[26:27]
	s_cbranch_execz .LBB0_454
	v_lshl_add_u64 v[32:33], v[144:145], 0, v[32:33]
	v_mov_b64_e32 v[36:37], v[232:233]
	v_mov_b64_e32 v[38:39], v[234:235]
	v_mov_b64_e32 v[48:49], v[228:229]
	v_mov_b64_e32 v[50:51], v[230:231]
	v_pk_mul_f32 v[54:55], v[16:17], v[36:37] op_sel:[1,1] op_sel_hi:[0,1]
	v_pk_mul_f32 v[52:53], v[20:21], v[48:49] op_sel:[1,1] op_sel_hi:[0,1]
	v_pk_mul_f32 v[32:33], v[20:21], v[48:49]
	v_pk_fma_f32 v[20:21], v[20:21], v[48:49], v[52:53] op_sel_hi:[1,0,1]
	s_nop 0
	v_mul_f32_e32 v20, v23, v51
	v_pk_fma_f32 v[48:49], v[22:23], v[50:51], v[20:21] op_sel_hi:[1,1,0] neg_lo:[0,0,1] neg_hi:[0,0,1]
	v_mul_f32_e32 v20, v22, v51
	v_pk_fma_f32 v[50:51], v[22:23], v[50:51], v[20:21] op_sel:[1,0,0] op_sel_hi:[0,1,0]
	v_pk_mul_f32 v[22:23], v[16:17], v[36:37]
	v_pk_fma_f32 v[16:17], v[16:17], v[36:37], v[54:55] op_sel_hi:[1,0,1]
	v_sub_f32_e32 v20, v32, v52
	v_mul_f32_e32 v16, v19, v39
	v_pk_fma_f32 v[36:37], v[18:19], v[38:39], v[16:17] op_sel_hi:[1,1,0] neg_lo:[0,0,1] neg_hi:[0,0,1]
	v_mul_f32_e32 v16, v18, v39
	v_pk_fma_f32 v[38:39], v[18:19], v[38:39], v[16:17] op_sel:[1,0,0] op_sel_hi:[0,1,0]
	v_sub_f32_e32 v16, v22, v54
	v_mov_b32_e32 v22, v48
	v_mov_b32_e32 v23, v50
	v_mov_b32_e32 v18, v36
	v_mov_b32_e32 v19, v38

.LBB0_459:
	v_add_u32_e32 v18, 0xb0, v136
	v_ashrrev_i32_e32 v19, 31, v18
	s_andn2_b64 vcc, exec, s[8:9]
	v_lshlrev_b64 v[8:9], 6, v[18:19]
	s_cbranch_vccnz .LBB0_465
	s_and_saveexec_b64 s[8:9], s[26:27]
	s_cbranch_execz .LBB0_462
	v_lshl_add_u64 v[32:33], v[144:145], 0, v[8:9]
	v_mov_b64_e32 v[20:21], v[240:241]
	v_mov_b64_e32 v[22:23], v[242:243]
	v_mov_b64_e32 v[32:33], v[236:237]
	v_mov_b64_e32 v[34:35], v[238:239]
	v_pk_mul_f32 v[40:41], v[10:11], v[20:21] op_sel:[1,1] op_sel_hi:[0,1]
	v_pk_mul_f32 v[38:39], v[12:13], v[32:33] op_sel:[1,1] op_sel_hi:[0,1]
	v_pk_mul_f32 v[36:37], v[12:13], v[32:33]
	v_pk_fma_f32 v[12:13], v[12:13], v[32:33], v[38:39] op_sel_hi:[1,0,1]
	s_nop 0
	v_mul_f32_e32 v12, v17, v35
	v_pk_fma_f32 v[32:33], v[16:17], v[34:35], v[12:13] op_sel_hi:[1,1,0] neg_lo:[0,0,1] neg_hi:[0,0,1]
	v_mul_f32_e32 v12, v16, v35
	v_pk_fma_f32 v[34:35], v[16:17], v[34:35], v[12:13] op_sel:[1,0,0] op_sel_hi:[0,1,0]
	v_pk_mul_f32 v[16:17], v[10:11], v[20:21]
	v_pk_fma_f32 v[10:11], v[10:11], v[20:21], v[40:41] op_sel_hi:[1,0,1]
	v_sub_f32_e32 v12, v36, v38
	v_mul_f32_e32 v10, v15, v23
	v_pk_fma_f32 v[20:21], v[14:15], v[22:23], v[10:11] op_sel_hi:[1,1,0] neg_lo:[0,0,1] neg_hi:[0,0,1]
	v_mul_f32_e32 v10, v14, v23
	v_pk_fma_f32 v[22:23], v[14:15], v[22:23], v[10:11] op_sel:[1,0,0] op_sel_hi:[0,1,0]
	v_sub_f32_e32 v10, v16, v40
	v_mov_b32_e32 v16, v32
	v_mov_b32_e32 v17, v34
	v_mov_b32_e32 v14, v20
	v_mov_b32_e32 v15, v22

.LBB0_469:
	s_andn2_b64 vcc, exec, s[6:7]
	s_cbranch_vccnz .LBB0_473
	s_and_saveexec_b64 s[4:5], s[26:27]
	s_cbranch_execz .LBB0_472
	v_lshl_add_u64 v[8:9], v[144:145], 0, v[8:9]
	v_mov_b64_e32 v[12:13], v[236:237]
	v_mov_b64_e32 v[14:15], v[238:239]
	v_mov_b64_e32 v[16:17], v[240:241]
	v_mov_b64_e32 v[18:19], v[242:243]
	v_pk_mul_f32 v[20:21], v[4:5], v[12:13] op_sel:[1,1] op_sel_hi:[0,1]
	v_mul_f32_e32 v22, v7, v15
	v_mul_f32_e32 v24, v6, v15
	v_pk_mul_f32 v[28:29], v[0:1], v[16:17] op_sel:[1,1] op_sel_hi:[0,1]
	v_mul_f32_e32 v30, v3, v19
	v_mul_f32_e32 v32, v2, v19
	v_pk_mul_f32 v[8:9], v[4:5], v[12:13]
	v_pk_mul_f32 v[26:27], v[0:1], v[16:17]
	v_pk_fma_f32 v[4:5], v[4:5], v[12:13], v[20:21] op_sel_hi:[1,0,1]
	v_pk_fma_f32 v[12:13], v[6:7], v[14:15], v[22:23] op_sel_hi:[1,1,0] neg_lo:[0,0,1] neg_hi:[0,0,1]
	v_pk_fma_f32 v[14:15], v[6:7], v[14:15], v[24:25] op_sel:[1,0,0] op_sel_hi:[0,1,0]
	v_pk_fma_f32 v[0:1], v[0:1], v[16:17], v[28:29] op_sel_hi:[1,0,1]
	v_pk_fma_f32 v[16:17], v[2:3], v[18:19], v[30:31] op_sel_hi:[1,1,0] neg_lo:[0,0,1] neg_hi:[0,0,1]
	v_pk_fma_f32 v[18:19], v[2:3], v[18:19], v[32:33] op_sel:[1,0,0] op_sel_hi:[0,1,0]
	v_sub_f32_e32 v4, v8, v20
	v_sub_f32_e32 v0, v26, v28
	v_mov_b32_e32 v6, v12
	v_mov_b32_e32 v7, v14
	v_mov_b32_e32 v2, v16
	v_mov_b32_e32 v3, v18

.LBB0_1156:
	v_mov_b32_e32 v248, v128
	v_ashrrev_i32_e32 v249, 31, v128
	v_lshl_or_b32 v250, s65, 8, v161
	v_lshlrev_b64 v[248:249], 14, v[248:249]
	v_ashrrev_i32_e32 v251, 31, v250
	v_lshl_add_u64 v[248:249], s[72:73], 0, v[248:249]
	v_lshl_add_u64 v[248:249], v[250:251], 2, v[248:249]
	global_load_dwordx4 v[232:235], v[248:249], off
	global_load_dwordx4 v[236:239], v[248:249], off offset:16
	global_load_dwordx4 v[240:243], v[248:249], off offset:512
	global_load_dwordx4 v[244:247], v[248:249], off offset:528
	s_mov_b32 s67, -2
	s_movk_i32 s68, 0x100

.LBB0_1160:
	v_lshl_or_b32 v148, s65, 8, v161
	v_ashrrev_i32_e32 v149, 31, v148
	s_nop 15
	s_nop 15
	v_add_u32_e32 v144, s39, v160
	v_cmp_gt_i32_e32 vcc, s38, v160
	v_ashrrev_i32_e32 v150, 1, v148
	v_add_u32_e32 v148, 0x80, v148
	v_cndmask_b32_e32 v144, -1, v144, vcc
	v_cmp_lt_i32_e32 vcc, -1, v144
	v_ashrrev_i32_e32 v151, 31, v150
	v_ashrrev_i32_e32 v148, 1, v148
	s_and_saveexec_b64 s[10:11], vcc
	s_cbranch_execz .LBB0_1162
	v_pk_fma_f32 v[124:125], v[124:125], s[20:21], v[232:233] op_sel_hi:[1,0,1]
	v_lshlrev_b64 v[176:177], 11, v[144:145]
	v_min_f32_e32 v124, 0x40e00000, v124
	v_mul_f32_e32 v144, 0x3fd9db23, v124
	v_mul_f32_e32 v144, 0xbfb8aa3b, v144
	v_exp_f32_e32 v144, v144
	v_pk_fma_f32 v[126:127], v[126:127], s[20:21], v[234:235] op_sel_hi:[1,0,1]
	v_pk_fma_f32 v[120:121], v[120:121], s[20:21], v[236:237] op_sel_hi:[1,0,1]
	v_min_f32_e32 v126, 0x40e00000, v126
	v_add_f32_e32 v144, 1.0, v144
	v_mul_f32_e32 v149, 0x3fd9db23, v126
	v_rcp_f32_e32 v144, v144
	v_mul_f32_e32 v149, 0xbfb8aa3b, v149
	v_exp_f32_e32 v149, v149
	v_med3_f32 v125, v125, s61, v172
	v_mul_f32_e32 v124, v124, v144
	v_add_f32_e32 v125, 1.0, v125
	v_min_f32_e32 v120, 0x40e00000, v120
	v_add_f32_e32 v144, 1.0, v149
	v_mul_f32_e32 v124, v125, v124
	v_med3_f32 v125, v127, s61, v172
	v_mul_f32_e32 v127, 0x3fd9db23, v120
	v_rcp_f32_e32 v144, v144
	v_mul_f32_e32 v127, 0xbfb8aa3b, v127
	v_exp_f32_e32 v127, v127
	v_pk_fma_f32 v[122:123], v[122:123], s[20:21], v[238:239] op_sel_hi:[1,0,1]
	v_mul_f32_e32 v126, v126, v144
	v_add_f32_e32 v125, 1.0, v125
	v_min_f32_e32 v122, 0x40e00000, v122
	v_mul_f32_e32 v125, v125, v126
	v_add_f32_e32 v126, 1.0, v127
	v_mul_f32_e32 v127, 0x3fd9db23, v122
	v_rcp_f32_e32 v126, v126
	v_mul_f32_e32 v127, 0xbfb8aa3b, v127
	v_exp_f32_e32 v127, v127
	v_med3_f32 v121, v121, s61, v172
	v_mul_f32_e32 v120, v120, v126
	v_add_f32_e32 v121, 1.0, v121
	v_mul_f32_e32 v120, v121, v120
	v_add_f32_e32 v121, 1.0, v127
	v_rcp_f32_e32 v121, v121
	v_mov_b32_e32 v126, v145
	v_cvt_pk_fp8_f32 v126, v124, v125
	v_med3_f32 v123, v123, s61, v172
	v_mul_f32_e32 v121, v122, v121
	v_add_f32_e32 v122, 1.0, v123
	v_pk_fma_f32 v[116:117], v[116:117], s[20:21], v[240:241] op_sel_hi:[1,0,1]
	v_mul_f32_e32 v121, v122, v121
	v_min_f32_e32 v116, 0x40e00000, v116
	v_cvt_pk_fp8_f32 v126, v120, v121 op_sel:[0,0,1]
	v_mul_f32_e32 v120, 0x3fd9db23, v116
	v_mul_f32_e32 v120, 0xbfb8aa3b, v120
	v_exp_f32_e32 v122, v120
	v_pk_fma_f32 v[118:119], v[118:119], s[20:21], v[242:243] op_sel_hi:[1,0,1]
	v_pk_fma_f32 v[112:113], v[112:113], s[20:21], v[244:245] op_sel_hi:[1,0,1]
	v_min_f32_e32 v118, 0x40e00000, v118
	v_add_f32_e32 v122, 1.0, v122
	v_mul_f32_e32 v123, 0x3fd9db23, v118
	v_rcp_f32_e32 v122, v122
	v_mul_f32_e32 v123, 0xbfb8aa3b, v123
	v_exp_f32_e32 v123, v123
	v_med3_f32 v117, v117, s61, v172
	v_mul_f32_e32 v116, v116, v122
	v_add_f32_e32 v117, 1.0, v117
	v_min_f32_e32 v112, 0x40e00000, v112
	v_add_f32_e32 v122, 1.0, v123
	v_mul_f32_e32 v116, v117, v116
	v_med3_f32 v117, v119, s61, v172
	v_mul_f32_e32 v119, 0x3fd9db23, v112
	v_rcp_f32_e32 v122, v122
	v_mul_f32_e32 v119, 0xbfb8aa3b, v119
	v_exp_f32_e32 v119, v119
	v_pk_fma_f32 v[114:115], v[114:115], s[20:21], v[246:247] op_sel_hi:[1,0,1]
	v_mul_f32_e32 v118, v118, v122
	v_add_f32_e32 v117, 1.0, v117
	v_min_f32_e32 v114, 0x40e00000, v114
	v_mul_f32_e32 v117, v117, v118
	v_add_f32_e32 v118, 1.0, v119
	v_mul_f32_e32 v119, 0x3fd9db23, v114
	v_rcp_f32_e32 v118, v118
	v_mul_f32_e32 v119, 0xbfb8aa3b, v119
	v_exp_f32_e32 v119, v119
	v_med3_f32 v113, v113, s61, v172
	v_mul_f32_e32 v112, v112, v118
	v_add_f32_e32 v113, 1.0, v113
	v_mul_f32_e32 v112, v113, v112
	v_add_f32_e32 v113, 1.0, v119
	v_rcp_f32_e32 v113, v113
	v_mov_b32_e32 v118, v145
	v_cvt_pk_fp8_f32 v118, v116, v117
	v_med3_f32 v115, v115, s61, v172
	v_mul_f32_e32 v113, v114, v113
	v_add_f32_e32 v114, 1.0, v115
	v_mul_f32_e32 v113, v114, v113
	v_cvt_pk_fp8_f32 v118, v112, v113 op_sel:[0,0,1]
	v_lshl_add_u64 v[176:177], s[16:17], 0, v[176:177]
	v_ashrrev_i32_e32 v149, 31, v148
	v_lshl_add_u64 v[120:121], v[176:177], 0, v[150:151]
	v_lshl_add_u64 v[112:113], v[176:177], 0, v[148:149]
	global_store_dword v[120:121], v126, off
	global_store_dword v[112:113], v118, off
.LBB0_1162:
	s_or_b64 exec, exec, s[10:11]
	v_add_u32_e32 v112, s39, v162
	v_cmp_gt_i32_e32 vcc, s38, v162
	s_nop 1
	v_cndmask_b32_e32 v144, -1, v112, vcc
	v_cmp_lt_i32_e32 vcc, -1, v144
	s_and_saveexec_b64 s[10:11], vcc
	s_cbranch_execz .LBB0_1164
	v_pk_fma_f32 v[108:109], v[108:109], s[20:21], v[232:233] op_sel_hi:[1,0,1]
	v_pk_fma_f32 v[110:111], v[110:111], s[20:21], v[234:235] op_sel_hi:[1,0,1]
	v_min_f32_e32 v108, 0x40e00000, v108
	v_mul_f32_e32 v114, 0x3fd9db23, v108
	v_mul_f32_e32 v114, 0xbfb8aa3b, v114
	v_exp_f32_e32 v114, v114
	v_min_f32_e32 v110, 0x40e00000, v110
	v_mul_f32_e32 v115, 0x3fd9db23, v110
	v_mul_f32_e32 v115, 0xbfb8aa3b, v115
	v_add_f32_e32 v114, 1.0, v114
	v_rcp_f32_e32 v114, v114
	v_exp_f32_e32 v115, v115
	v_pk_fma_f32 v[104:105], v[104:105], s[20:21], v[236:237] op_sel_hi:[1,0,1]
	v_med3_f32 v109, v109, s61, v172
	v_mul_f32_e32 v108, v108, v114
	v_add_f32_e32 v109, 1.0, v109
	v_min_f32_e32 v104, 0x40e00000, v104
	v_add_f32_e32 v114, 1.0, v115
	v_mul_f32_e32 v108, v109, v108
	v_med3_f32 v109, v111, s61, v172
	v_mul_f32_e32 v111, 0x3fd9db23, v104
	v_rcp_f32_e32 v114, v114
	v_mul_f32_e32 v111, 0xbfb8aa3b, v111
	v_exp_f32_e32 v111, v111
	v_pk_fma_f32 v[106:107], v[106:107], s[20:21], v[238:239] op_sel_hi:[1,0,1]
	v_mul_f32_e32 v110, v110, v114
	v_add_f32_e32 v109, 1.0, v109
	v_min_f32_e32 v106, 0x40e00000, v106
	v_mul_f32_e32 v109, v109, v110
	v_add_f32_e32 v110, 1.0, v111
	v_mul_f32_e32 v111, 0x3fd9db23, v106
	v_rcp_f32_e32 v110, v110
	v_mul_f32_e32 v111, 0xbfb8aa3b, v111
	v_exp_f32_e32 v111, v111
	v_med3_f32 v105, v105, s61, v172
	v_mul_f32_e32 v104, v104, v110
	v_add_f32_e32 v105, 1.0, v105
	v_mul_f32_e32 v104, v105, v104
	v_add_f32_e32 v105, 1.0, v111
	v_rcp_f32_e32 v105, v105
	v_mov_b32_e32 v110, v145
	v_cvt_pk_fp8_f32 v110, v108, v109
	v_med3_f32 v107, v107, s61, v172
	v_mul_f32_e32 v105, v106, v105
	v_add_f32_e32 v106, 1.0, v107
	v_pk_fma_f32 v[100:101], v[100:101], s[20:21], v[240:241] op_sel_hi:[1,0,1]
	v_mul_f32_e32 v105, v106, v105
	v_min_f32_e32 v100, 0x40e00000, v100
	v_cvt_pk_fp8_f32 v110, v104, v105 op_sel:[0,0,1]
	v_mul_f32_e32 v104, 0x3fd9db23, v100
	v_mul_f32_e32 v104, 0xbfb8aa3b, v104
	v_exp_f32_e32 v106, v104
	v_pk_fma_f32 v[102:103], v[102:103], s[20:21], v[242:243] op_sel_hi:[1,0,1]
	v_pk_fma_f32 v[96:97], v[96:97], s[20:21], v[244:245] op_sel_hi:[1,0,1]
	v_min_f32_e32 v102, 0x40e00000, v102
	v_add_f32_e32 v106, 1.0, v106
	v_mul_f32_e32 v107, 0x3fd9db23, v102
	v_rcp_f32_e32 v106, v106
	v_mul_f32_e32 v107, 0xbfb8aa3b, v107
	v_exp_f32_e32 v107, v107
	v_med3_f32 v101, v101, s61, v172
	v_mul_f32_e32 v100, v100, v106
	v_add_f32_e32 v101, 1.0, v101
	v_min_f32_e32 v96, 0x40e00000, v96
	v_add_f32_e32 v106, 1.0, v107
	v_mul_f32_e32 v100, v101, v100
	v_med3_f32 v101, v103, s61, v172
	v_mul_f32_e32 v103, 0x3fd9db23, v96
	v_rcp_f32_e32 v106, v106
	v_mul_f32_e32 v103, 0xbfb8aa3b, v103
	v_exp_f32_e32 v103, v103
	v_pk_fma_f32 v[98:99], v[98:99], s[20:21], v[246:247] op_sel_hi:[1,0,1]
	v_mul_f32_e32 v102, v102, v106
	v_add_f32_e32 v101, 1.0, v101
	v_min_f32_e32 v98, 0x40e00000, v98
	v_mul_f32_e32 v101, v101, v102
	v_add_f32_e32 v102, 1.0, v103
	v_mul_f32_e32 v103, 0x3fd9db23, v98
	v_rcp_f32_e32 v102, v102
	v_mul_f32_e32 v103, 0xbfb8aa3b, v103
	v_exp_f32_e32 v103, v103
	v_med3_f32 v97, v97, s61, v172
	v_mul_f32_e32 v96, v96, v102
	v_add_f32_e32 v97, 1.0, v97
	v_mul_f32_e32 v96, v97, v96
	v_add_f32_e32 v97, 1.0, v103
	v_rcp_f32_e32 v97, v97
	v_mov_b32_e32 v102, v145
	v_cvt_pk_fp8_f32 v102, v100, v101
	v_med3_f32 v99, v99, s61, v172
	v_mul_f32_e32 v97, v98, v97
	v_add_f32_e32 v98, 1.0, v99
	v_mul_f32_e32 v97, v98, v97
	v_cvt_pk_fp8_f32 v102, v96, v97 op_sel:[0,0,1]
	v_lshlrev_b64 v[112:113], 11, v[144:145]
	v_lshl_add_u64 v[112:113], s[16:17], 0, v[112:113]
	v_ashrrev_i32_e32 v149, 31, v148
	v_lshl_add_u64 v[104:105], v[112:113], 0, v[150:151]
	v_lshl_add_u64 v[96:97], v[112:113], 0, v[148:149]
	global_store_dword v[104:105], v110, off
	global_store_dword v[96:97], v102, off
.LBB0_1164:
	s_or_b64 exec, exec, s[10:11]
	v_add_u32_e32 v96, s39, v163
	v_cmp_gt_i32_e32 vcc, s38, v163
	s_nop 1
	v_cndmask_b32_e32 v144, -1, v96, vcc
	v_cmp_lt_i32_e32 vcc, -1, v144
	s_and_saveexec_b64 s[10:11], vcc
	s_cbranch_execz .LBB0_1166
	v_pk_fma_f32 v[92:93], v[92:93], s[20:21], v[232:233] op_sel_hi:[1,0,1]
	v_pk_fma_f32 v[94:95], v[94:95], s[20:21], v[234:235] op_sel_hi:[1,0,1]
	v_min_f32_e32 v92, 0x40e00000, v92
	v_mul_f32_e32 v98, 0x3fd9db23, v92
	v_mul_f32_e32 v98, 0xbfb8aa3b, v98
	v_exp_f32_e32 v98, v98
	v_min_f32_e32 v94, 0x40e00000, v94
	v_mul_f32_e32 v99, 0x3fd9db23, v94
	v_mul_f32_e32 v99, 0xbfb8aa3b, v99
	v_add_f32_e32 v98, 1.0, v98
	v_rcp_f32_e32 v98, v98
	v_exp_f32_e32 v99, v99
	v_pk_fma_f32 v[88:89], v[88:89], s[20:21], v[236:237] op_sel_hi:[1,0,1]
	v_med3_f32 v93, v93, s61, v172
	v_mul_f32_e32 v92, v92, v98
	v_add_f32_e32 v93, 1.0, v93
	v_min_f32_e32 v88, 0x40e00000, v88
	v_add_f32_e32 v98, 1.0, v99
	v_mul_f32_e32 v92, v93, v92
	v_med3_f32 v93, v95, s61, v172
	v_mul_f32_e32 v95, 0x3fd9db23, v88
	v_rcp_f32_e32 v98, v98
	v_mul_f32_e32 v95, 0xbfb8aa3b, v95
	v_exp_f32_e32 v95, v95
	v_pk_fma_f32 v[90:91], v[90:91], s[20:21], v[238:239] op_sel_hi:[1,0,1]
	v_mul_f32_e32 v94, v94, v98
	v_add_f32_e32 v93, 1.0, v93
	v_min_f32_e32 v90, 0x40e00000, v90
	v_mul_f32_e32 v93, v93, v94
	v_add_f32_e32 v94, 1.0, v95
	v_mul_f32_e32 v95, 0x3fd9db23, v90
	v_rcp_f32_e32 v94, v94
	v_mul_f32_e32 v95, 0xbfb8aa3b, v95
	v_exp_f32_e32 v95, v95
	v_med3_f32 v89, v89, s61, v172
	v_mul_f32_e32 v88, v88, v94
	v_add_f32_e32 v89, 1.0, v89
	v_mul_f32_e32 v88, v89, v88
	v_add_f32_e32 v89, 1.0, v95
	v_rcp_f32_e32 v89, v89
	v_mov_b32_e32 v94, v145
	v_cvt_pk_fp8_f32 v94, v92, v93
	v_med3_f32 v91, v91, s61, v172
	v_mul_f32_e32 v89, v90, v89
	v_add_f32_e32 v90, 1.0, v91
	v_pk_fma_f32 v[84:85], v[84:85], s[20:21], v[240:241] op_sel_hi:[1,0,1]
	v_mul_f32_e32 v89, v90, v89
	v_min_f32_e32 v84, 0x40e00000, v84
	v_cvt_pk_fp8_f32 v94, v88, v89 op_sel:[0,0,1]
	v_mul_f32_e32 v88, 0x3fd9db23, v84
	v_mul_f32_e32 v88, 0xbfb8aa3b, v88
	v_exp_f32_e32 v90, v88
	v_pk_fma_f32 v[86:87], v[86:87], s[20:21], v[242:243] op_sel_hi:[1,0,1]
	v_pk_fma_f32 v[80:81], v[80:81], s[20:21], v[244:245] op_sel_hi:[1,0,1]
	v_min_f32_e32 v86, 0x40e00000, v86
	v_add_f32_e32 v90, 1.0, v90
	v_mul_f32_e32 v91, 0x3fd9db23, v86
	v_rcp_f32_e32 v90, v90
	v_mul_f32_e32 v91, 0xbfb8aa3b, v91
	v_exp_f32_e32 v91, v91
	v_med3_f32 v85, v85, s61, v172
	v_mul_f32_e32 v84, v84, v90
	v_add_f32_e32 v85, 1.0, v85
	v_min_f32_e32 v80, 0x40e00000, v80
	v_add_f32_e32 v90, 1.0, v91
	v_mul_f32_e32 v84, v85, v84
	v_med3_f32 v85, v87, s61, v172
	v_mul_f32_e32 v87, 0x3fd9db23, v80
	v_rcp_f32_e32 v90, v90
	v_mul_f32_e32 v87, 0xbfb8aa3b, v87
	v_exp_f32_e32 v87, v87
	v_pk_fma_f32 v[82:83], v[82:83], s[20:21], v[246:247] op_sel_hi:[1,0,1]
	v_mul_f32_e32 v86, v86, v90
	v_add_f32_e32 v85, 1.0, v85
	v_min_f32_e32 v82, 0x40e00000, v82
	v_mul_f32_e32 v85, v85, v86
	v_add_f32_e32 v86, 1.0, v87
	v_mul_f32_e32 v87, 0x3fd9db23, v82
	v_rcp_f32_e32 v86, v86
	v_mul_f32_e32 v87, 0xbfb8aa3b, v87
	v_exp_f32_e32 v87, v87
	v_med3_f32 v81, v81, s61, v172
	v_mul_f32_e32 v80, v80, v86
	v_add_f32_e32 v81, 1.0, v81
	v_mul_f32_e32 v80, v81, v80
	v_add_f32_e32 v81, 1.0, v87
	v_rcp_f32_e32 v81, v81
	v_mov_b32_e32 v86, v145
	v_cvt_pk_fp8_f32 v86, v84, v85
	v_med3_f32 v83, v83, s61, v172
	v_mul_f32_e32 v81, v82, v81
	v_add_f32_e32 v82, 1.0, v83
	v_mul_f32_e32 v81, v82, v81
	v_cvt_pk_fp8_f32 v86, v80, v81 op_sel:[0,0,1]
	v_lshlrev_b64 v[96:97], 11, v[144:145]
	v_lshl_add_u64 v[96:97], s[16:17], 0, v[96:97]
	v_ashrrev_i32_e32 v149, 31, v148
	v_lshl_add_u64 v[88:89], v[96:97], 0, v[150:151]
	v_lshl_add_u64 v[80:81], v[96:97], 0, v[148:149]
	global_store_dword v[88:89], v94, off
	global_store_dword v[80:81], v86, off
.LBB0_1166:
	s_or_b64 exec, exec, s[10:11]
	v_add_u32_e32 v80, s39, v164
	v_cmp_gt_i32_e32 vcc, s38, v164
	s_nop 1
	v_cndmask_b32_e32 v144, -1, v80, vcc
	v_cmp_lt_i32_e32 vcc, -1, v144
	s_and_saveexec_b64 s[10:11], vcc
	s_cbranch_execz .LBB0_1168
	v_pk_fma_f32 v[76:77], v[76:77], s[20:21], v[232:233] op_sel_hi:[1,0,1]
	v_pk_fma_f32 v[78:79], v[78:79], s[20:21], v[234:235] op_sel_hi:[1,0,1]
	v_min_f32_e32 v76, 0x40e00000, v76
	v_mul_f32_e32 v82, 0x3fd9db23, v76
	v_mul_f32_e32 v82, 0xbfb8aa3b, v82
	v_exp_f32_e32 v82, v82
	v_min_f32_e32 v78, 0x40e00000, v78
	v_mul_f32_e32 v83, 0x3fd9db23, v78
	v_mul_f32_e32 v83, 0xbfb8aa3b, v83
	v_add_f32_e32 v82, 1.0, v82
	v_rcp_f32_e32 v82, v82
	v_exp_f32_e32 v83, v83
	v_pk_fma_f32 v[72:73], v[72:73], s[20:21], v[236:237] op_sel_hi:[1,0,1]
	v_med3_f32 v77, v77, s61, v172
	v_mul_f32_e32 v76, v76, v82
	v_add_f32_e32 v77, 1.0, v77
	v_min_f32_e32 v72, 0x40e00000, v72
	v_add_f32_e32 v82, 1.0, v83
	v_mul_f32_e32 v76, v77, v76
	v_med3_f32 v77, v79, s61, v172
	v_mul_f32_e32 v79, 0x3fd9db23, v72
	v_rcp_f32_e32 v82, v82
	v_mul_f32_e32 v79, 0xbfb8aa3b, v79
	v_exp_f32_e32 v79, v79
	v_pk_fma_f32 v[74:75], v[74:75], s[20:21], v[238:239] op_sel_hi:[1,0,1]
	v_mul_f32_e32 v78, v78, v82
	v_add_f32_e32 v77, 1.0, v77
	v_min_f32_e32 v74, 0x40e00000, v74
	v_mul_f32_e32 v77, v77, v78
	v_add_f32_e32 v78, 1.0, v79
	v_mul_f32_e32 v79, 0x3fd9db23, v74
	v_rcp_f32_e32 v78, v78
	v_mul_f32_e32 v79, 0xbfb8aa3b, v79
	v_exp_f32_e32 v79, v79
	v_med3_f32 v73, v73, s61, v172
	v_mul_f32_e32 v72, v72, v78
	v_add_f32_e32 v73, 1.0, v73
	v_mul_f32_e32 v72, v73, v72
	v_add_f32_e32 v73, 1.0, v79
	v_rcp_f32_e32 v73, v73
	v_mov_b32_e32 v78, v145
	v_cvt_pk_fp8_f32 v78, v76, v77
	v_med3_f32 v75, v75, s61, v172
	v_mul_f32_e32 v73, v74, v73
	v_add_f32_e32 v74, 1.0, v75
	v_pk_fma_f32 v[68:69], v[68:69], s[20:21], v[240:241] op_sel_hi:[1,0,1]
	v_mul_f32_e32 v73, v74, v73
	v_min_f32_e32 v68, 0x40e00000, v68
	v_cvt_pk_fp8_f32 v78, v72, v73 op_sel:[0,0,1]
	v_mul_f32_e32 v72, 0x3fd9db23, v68
	v_mul_f32_e32 v72, 0xbfb8aa3b, v72
	v_exp_f32_e32 v74, v72
	v_pk_fma_f32 v[70:71], v[70:71], s[20:21], v[242:243] op_sel_hi:[1,0,1]
	v_pk_fma_f32 v[64:65], v[64:65], s[20:21], v[244:245] op_sel_hi:[1,0,1]
	v_min_f32_e32 v70, 0x40e00000, v70
	v_add_f32_e32 v74, 1.0, v74
	v_mul_f32_e32 v75, 0x3fd9db23, v70
	v_rcp_f32_e32 v74, v74
	v_mul_f32_e32 v75, 0xbfb8aa3b, v75
	v_exp_f32_e32 v75, v75
	v_med3_f32 v69, v69, s61, v172
	v_mul_f32_e32 v68, v68, v74
	v_add_f32_e32 v69, 1.0, v69
	v_min_f32_e32 v64, 0x40e00000, v64
	v_add_f32_e32 v74, 1.0, v75
	v_mul_f32_e32 v68, v69, v68
	v_med3_f32 v69, v71, s61, v172
	v_mul_f32_e32 v71, 0x3fd9db23, v64
	v_rcp_f32_e32 v74, v74
	v_mul_f32_e32 v71, 0xbfb8aa3b, v71
	v_exp_f32_e32 v71, v71
	v_pk_fma_f32 v[66:67], v[66:67], s[20:21], v[246:247] op_sel_hi:[1,0,1]
	v_mul_f32_e32 v70, v70, v74
	v_add_f32_e32 v69, 1.0, v69
	v_min_f32_e32 v66, 0x40e00000, v66
	v_mul_f32_e32 v69, v69, v70
	v_add_f32_e32 v70, 1.0, v71
	v_mul_f32_e32 v71, 0x3fd9db23, v66
	v_rcp_f32_e32 v70, v70
	v_mul_f32_e32 v71, 0xbfb8aa3b, v71
	v_exp_f32_e32 v71, v71
	v_med3_f32 v65, v65, s61, v172
	v_mul_f32_e32 v64, v64, v70
	v_add_f32_e32 v65, 1.0, v65
	v_mul_f32_e32 v64, v65, v64
	v_add_f32_e32 v65, 1.0, v71
	v_rcp_f32_e32 v65, v65
	v_mov_b32_e32 v70, v145
	v_cvt_pk_fp8_f32 v70, v68, v69
	v_med3_f32 v67, v67, s61, v172
	v_mul_f32_e32 v65, v66, v65
	v_add_f32_e32 v66, 1.0, v67
	v_mul_f32_e32 v65, v66, v65
	v_cvt_pk_fp8_f32 v70, v64, v65 op_sel:[0,0,1]
	v_lshlrev_b64 v[80:81], 11, v[144:145]
	v_lshl_add_u64 v[80:81], s[16:17], 0, v[80:81]
	v_ashrrev_i32_e32 v149, 31, v148
	v_lshl_add_u64 v[72:73], v[80:81], 0, v[150:151]
	v_lshl_add_u64 v[64:65], v[80:81], 0, v[148:149]
	global_store_dword v[72:73], v78, off
	global_store_dword v[64:65], v70, off
.LBB0_1168:
	s_or_b64 exec, exec, s[10:11]
	v_add_u32_e32 v64, s39, v165
	v_cmp_gt_i32_e32 vcc, s38, v165
	s_nop 1
	v_cndmask_b32_e32 v144, -1, v64, vcc
	v_cmp_lt_i32_e32 vcc, -1, v144
	s_and_saveexec_b64 s[10:11], vcc
	s_cbranch_execz .LBB0_1170
	v_pk_fma_f32 v[60:61], v[60:61], s[20:21], v[232:233] op_sel_hi:[1,0,1]
	v_pk_fma_f32 v[62:63], v[62:63], s[20:21], v[234:235] op_sel_hi:[1,0,1]
	v_min_f32_e32 v60, 0x40e00000, v60
	v_mul_f32_e32 v66, 0x3fd9db23, v60
	v_mul_f32_e32 v66, 0xbfb8aa3b, v66
	v_exp_f32_e32 v66, v66
	v_min_f32_e32 v62, 0x40e00000, v62
	v_mul_f32_e32 v67, 0x3fd9db23, v62
	v_mul_f32_e32 v67, 0xbfb8aa3b, v67
	v_add_f32_e32 v66, 1.0, v66
	v_rcp_f32_e32 v66, v66
	v_exp_f32_e32 v67, v67
	v_pk_fma_f32 v[56:57], v[56:57], s[20:21], v[236:237] op_sel_hi:[1,0,1]
	v_med3_f32 v61, v61, s61, v172
	v_mul_f32_e32 v60, v60, v66
	v_add_f32_e32 v61, 1.0, v61
	v_min_f32_e32 v56, 0x40e00000, v56
	v_add_f32_e32 v66, 1.0, v67
	v_mul_f32_e32 v60, v61, v60
	v_med3_f32 v61, v63, s61, v172
	v_mul_f32_e32 v63, 0x3fd9db23, v56
	v_rcp_f32_e32 v66, v66
	v_mul_f32_e32 v63, 0xbfb8aa3b, v63
	v_exp_f32_e32 v63, v63
	v_pk_fma_f32 v[58:59], v[58:59], s[20:21], v[238:239] op_sel_hi:[1,0,1]
	v_mul_f32_e32 v62, v62, v66
	v_add_f32_e32 v61, 1.0, v61
	v_min_f32_e32 v58, 0x40e00000, v58
	v_mul_f32_e32 v61, v61, v62
	v_add_f32_e32 v62, 1.0, v63
	v_mul_f32_e32 v63, 0x3fd9db23, v58
	v_rcp_f32_e32 v62, v62
	v_mul_f32_e32 v63, 0xbfb8aa3b, v63
	v_exp_f32_e32 v63, v63
	v_med3_f32 v57, v57, s61, v172
	v_mul_f32_e32 v56, v56, v62
	v_add_f32_e32 v57, 1.0, v57
	v_mul_f32_e32 v56, v57, v56
	v_add_f32_e32 v57, 1.0, v63
	v_rcp_f32_e32 v57, v57
	v_mov_b32_e32 v62, v145
	v_cvt_pk_fp8_f32 v62, v60, v61
	v_med3_f32 v59, v59, s61, v172
	v_mul_f32_e32 v57, v58, v57
	v_add_f32_e32 v58, 1.0, v59
	v_pk_fma_f32 v[52:53], v[52:53], s[20:21], v[240:241] op_sel_hi:[1,0,1]
	v_mul_f32_e32 v57, v58, v57
	v_min_f32_e32 v52, 0x40e00000, v52
	v_cvt_pk_fp8_f32 v62, v56, v57 op_sel:[0,0,1]
	v_mul_f32_e32 v56, 0x3fd9db23, v52
	v_mul_f32_e32 v56, 0xbfb8aa3b, v56
	v_exp_f32_e32 v58, v56
	v_pk_fma_f32 v[54:55], v[54:55], s[20:21], v[242:243] op_sel_hi:[1,0,1]
	v_pk_fma_f32 v[48:49], v[48:49], s[20:21], v[244:245] op_sel_hi:[1,0,1]
	v_min_f32_e32 v54, 0x40e00000, v54
	v_add_f32_e32 v58, 1.0, v58
	v_mul_f32_e32 v59, 0x3fd9db23, v54
	v_rcp_f32_e32 v58, v58
	v_mul_f32_e32 v59, 0xbfb8aa3b, v59
	v_exp_f32_e32 v59, v59
	v_med3_f32 v53, v53, s61, v172
	v_mul_f32_e32 v52, v52, v58
	v_add_f32_e32 v53, 1.0, v53
	v_min_f32_e32 v48, 0x40e00000, v48
	v_add_f32_e32 v58, 1.0, v59
	v_mul_f32_e32 v52, v53, v52
	v_med3_f32 v53, v55, s61, v172
	v_mul_f32_e32 v55, 0x3fd9db23, v48
	v_rcp_f32_e32 v58, v58
	v_mul_f32_e32 v55, 0xbfb8aa3b, v55
	v_exp_f32_e32 v55, v55
	v_pk_fma_f32 v[50:51], v[50:51], s[20:21], v[246:247] op_sel_hi:[1,0,1]
	v_mul_f32_e32 v54, v54, v58
	v_add_f32_e32 v53, 1.0, v53
	v_min_f32_e32 v50, 0x40e00000, v50
	v_mul_f32_e32 v53, v53, v54
	v_add_f32_e32 v54, 1.0, v55
	v_mul_f32_e32 v55, 0x3fd9db23, v50
	v_rcp_f32_e32 v54, v54
	v_mul_f32_e32 v55, 0xbfb8aa3b, v55
	v_exp_f32_e32 v55, v55
	v_med3_f32 v49, v49, s61, v172
	v_mul_f32_e32 v48, v48, v54
	v_add_f32_e32 v49, 1.0, v49
	v_mul_f32_e32 v48, v49, v48
	v_add_f32_e32 v49, 1.0, v55
	v_rcp_f32_e32 v49, v49
	v_mov_b32_e32 v54, v145
	v_cvt_pk_fp8_f32 v54, v52, v53
	v_med3_f32 v51, v51, s61, v172
	v_mul_f32_e32 v49, v50, v49
	v_add_f32_e32 v50, 1.0, v51
	v_mul_f32_e32 v49, v50, v49
	v_cvt_pk_fp8_f32 v54, v48, v49 op_sel:[0,0,1]
	v_lshlrev_b64 v[64:65], 11, v[144:145]
	v_lshl_add_u64 v[64:65], s[16:17], 0, v[64:65]
	v_ashrrev_i32_e32 v149, 31, v148
	v_lshl_add_u64 v[56:57], v[64:65], 0, v[150:151]
	v_lshl_add_u64 v[48:49], v[64:65], 0, v[148:149]
	global_store_dword v[56:57], v62, off
	global_store_dword v[48:49], v54, off
.LBB0_1170:
	s_or_b64 exec, exec, s[10:11]
	v_add_u32_e32 v48, s39, v166
	v_cmp_gt_i32_e32 vcc, s38, v166
	s_nop 1
	v_cndmask_b32_e32 v144, -1, v48, vcc
	v_cmp_lt_i32_e32 vcc, -1, v144
	s_and_saveexec_b64 s[10:11], vcc
	s_cbranch_execz .LBB0_1172
	v_pk_fma_f32 v[44:45], v[44:45], s[20:21], v[232:233] op_sel_hi:[1,0,1]
	v_pk_fma_f32 v[46:47], v[46:47], s[20:21], v[234:235] op_sel_hi:[1,0,1]
	v_min_f32_e32 v44, 0x40e00000, v44
	v_mul_f32_e32 v50, 0x3fd9db23, v44
	v_mul_f32_e32 v50, 0xbfb8aa3b, v50
	v_exp_f32_e32 v50, v50
	v_min_f32_e32 v46, 0x40e00000, v46
	v_mul_f32_e32 v51, 0x3fd9db23, v46
	v_mul_f32_e32 v51, 0xbfb8aa3b, v51
	v_add_f32_e32 v50, 1.0, v50
	v_rcp_f32_e32 v50, v50
	v_exp_f32_e32 v51, v51
	v_pk_fma_f32 v[40:41], v[40:41], s[20:21], v[236:237] op_sel_hi:[1,0,1]
	v_med3_f32 v45, v45, s61, v172
	v_mul_f32_e32 v44, v44, v50
	v_add_f32_e32 v45, 1.0, v45
	v_min_f32_e32 v40, 0x40e00000, v40
	v_add_f32_e32 v50, 1.0, v51
	v_mul_f32_e32 v44, v45, v44
	v_med3_f32 v45, v47, s61, v172
	v_mul_f32_e32 v47, 0x3fd9db23, v40
	v_rcp_f32_e32 v50, v50
	v_mul_f32_e32 v47, 0xbfb8aa3b, v47
	v_exp_f32_e32 v47, v47
	v_pk_fma_f32 v[42:43], v[42:43], s[20:21], v[238:239] op_sel_hi:[1,0,1]
	v_mul_f32_e32 v46, v46, v50
	v_add_f32_e32 v45, 1.0, v45
	v_min_f32_e32 v42, 0x40e00000, v42
	v_mul_f32_e32 v45, v45, v46
	v_add_f32_e32 v46, 1.0, v47
	v_mul_f32_e32 v47, 0x3fd9db23, v42
	v_rcp_f32_e32 v46, v46
	v_mul_f32_e32 v47, 0xbfb8aa3b, v47
	v_exp_f32_e32 v47, v47
	v_med3_f32 v41, v41, s61, v172
	v_mul_f32_e32 v40, v40, v46
	v_add_f32_e32 v41, 1.0, v41
	v_mul_f32_e32 v40, v41, v40
	v_add_f32_e32 v41, 1.0, v47
	v_rcp_f32_e32 v41, v41
	v_mov_b32_e32 v46, v145
	v_cvt_pk_fp8_f32 v46, v44, v45
	v_med3_f32 v43, v43, s61, v172
	v_mul_f32_e32 v41, v42, v41
	v_add_f32_e32 v42, 1.0, v43
	v_pk_fma_f32 v[36:37], v[36:37], s[20:21], v[240:241] op_sel_hi:[1,0,1]
	v_mul_f32_e32 v41, v42, v41
	v_min_f32_e32 v36, 0x40e00000, v36
	v_cvt_pk_fp8_f32 v46, v40, v41 op_sel:[0,0,1]
	v_mul_f32_e32 v40, 0x3fd9db23, v36
	v_mul_f32_e32 v40, 0xbfb8aa3b, v40
	v_exp_f32_e32 v42, v40
	v_pk_fma_f32 v[38:39], v[38:39], s[20:21], v[242:243] op_sel_hi:[1,0,1]
	v_pk_fma_f32 v[32:33], v[32:33], s[20:21], v[244:245] op_sel_hi:[1,0,1]
	v_min_f32_e32 v38, 0x40e00000, v38
	v_add_f32_e32 v42, 1.0, v42
	v_mul_f32_e32 v43, 0x3fd9db23, v38
	v_rcp_f32_e32 v42, v42
	v_mul_f32_e32 v43, 0xbfb8aa3b, v43
	v_exp_f32_e32 v43, v43
	v_med3_f32 v37, v37, s61, v172
	v_mul_f32_e32 v36, v36, v42
	v_add_f32_e32 v37, 1.0, v37
	v_min_f32_e32 v32, 0x40e00000, v32
	v_add_f32_e32 v42, 1.0, v43
	v_mul_f32_e32 v36, v37, v36
	v_med3_f32 v37, v39, s61, v172
	v_mul_f32_e32 v39, 0x3fd9db23, v32
	v_rcp_f32_e32 v42, v42
	v_mul_f32_e32 v39, 0xbfb8aa3b, v39
	v_exp_f32_e32 v39, v39
	v_pk_fma_f32 v[34:35], v[34:35], s[20:21], v[246:247] op_sel_hi:[1,0,1]
	v_mul_f32_e32 v38, v38, v42
	v_add_f32_e32 v37, 1.0, v37
	v_min_f32_e32 v34, 0x40e00000, v34
	v_mul_f32_e32 v37, v37, v38
	v_add_f32_e32 v38, 1.0, v39
	v_mul_f32_e32 v39, 0x3fd9db23, v34
	v_rcp_f32_e32 v38, v38
	v_mul_f32_e32 v39, 0xbfb8aa3b, v39
	v_exp_f32_e32 v39, v39
	v_med3_f32 v33, v33, s61, v172
	v_mul_f32_e32 v32, v32, v38
	v_add_f32_e32 v33, 1.0, v33
	v_mul_f32_e32 v32, v33, v32
	v_add_f32_e32 v33, 1.0, v39
	v_rcp_f32_e32 v33, v33
	v_mov_b32_e32 v38, v145
	v_cvt_pk_fp8_f32 v38, v36, v37
	v_med3_f32 v35, v35, s61, v172
	v_mul_f32_e32 v33, v34, v33
	v_add_f32_e32 v34, 1.0, v35
	v_mul_f32_e32 v33, v34, v33
	v_cvt_pk_fp8_f32 v38, v32, v33 op_sel:[0,0,1]
	v_lshlrev_b64 v[48:49], 11, v[144:145]
	v_lshl_add_u64 v[48:49], s[16:17], 0, v[48:49]
	v_ashrrev_i32_e32 v149, 31, v148
	v_lshl_add_u64 v[40:41], v[48:49], 0, v[150:151]
	v_lshl_add_u64 v[32:33], v[48:49], 0, v[148:149]
	global_store_dword v[40:41], v46, off
	global_store_dword v[32:33], v38, off
.LBB0_1172:
	s_or_b64 exec, exec, s[10:11]
	v_add_u32_e32 v32, s39, v167
	v_cmp_gt_i32_e32 vcc, s38, v167
	s_nop 1
	v_cndmask_b32_e32 v144, -1, v32, vcc
	v_cmp_lt_i32_e32 vcc, -1, v144
	s_and_saveexec_b64 s[10:11], vcc
	s_cbranch_execz .LBB0_1174
	v_pk_fma_f32 v[28:29], v[28:29], s[20:21], v[232:233] op_sel_hi:[1,0,1]
	v_pk_fma_f32 v[30:31], v[30:31], s[20:21], v[234:235] op_sel_hi:[1,0,1]
	v_min_f32_e32 v28, 0x40e00000, v28
	v_mul_f32_e32 v34, 0x3fd9db23, v28
	v_mul_f32_e32 v34, 0xbfb8aa3b, v34
	v_exp_f32_e32 v34, v34
	v_min_f32_e32 v30, 0x40e00000, v30
	v_mul_f32_e32 v35, 0x3fd9db23, v30
	v_mul_f32_e32 v35, 0xbfb8aa3b, v35
	v_add_f32_e32 v34, 1.0, v34
	v_rcp_f32_e32 v34, v34
	v_exp_f32_e32 v35, v35
	v_pk_fma_f32 v[24:25], v[24:25], s[20:21], v[236:237] op_sel_hi:[1,0,1]
	v_med3_f32 v29, v29, s61, v172
	v_mul_f32_e32 v28, v28, v34
	v_add_f32_e32 v29, 1.0, v29
	v_min_f32_e32 v24, 0x40e00000, v24
	v_add_f32_e32 v34, 1.0, v35
	v_mul_f32_e32 v28, v29, v28
	v_med3_f32 v29, v31, s61, v172
	v_mul_f32_e32 v31, 0x3fd9db23, v24
	v_rcp_f32_e32 v34, v34
	v_mul_f32_e32 v31, 0xbfb8aa3b, v31
	v_exp_f32_e32 v31, v31
	v_pk_fma_f32 v[26:27], v[26:27], s[20:21], v[238:239] op_sel_hi:[1,0,1]
	v_mul_f32_e32 v30, v30, v34
	v_add_f32_e32 v29, 1.0, v29
	v_min_f32_e32 v26, 0x40e00000, v26
	v_mul_f32_e32 v29, v29, v30
	v_add_f32_e32 v30, 1.0, v31
	v_mul_f32_e32 v31, 0x3fd9db23, v26
	v_rcp_f32_e32 v30, v30
	v_mul_f32_e32 v31, 0xbfb8aa3b, v31
	v_exp_f32_e32 v31, v31
	v_med3_f32 v25, v25, s61, v172
	v_mul_f32_e32 v24, v24, v30
	v_add_f32_e32 v25, 1.0, v25
	v_mul_f32_e32 v24, v25, v24
	v_add_f32_e32 v25, 1.0, v31
	v_rcp_f32_e32 v25, v25
	v_mov_b32_e32 v30, v145
	v_cvt_pk_fp8_f32 v30, v28, v29
	v_med3_f32 v27, v27, s61, v172
	v_mul_f32_e32 v25, v26, v25
	v_add_f32_e32 v26, 1.0, v27
	v_pk_fma_f32 v[20:21], v[20:21], s[20:21], v[240:241] op_sel_hi:[1,0,1]
	v_mul_f32_e32 v25, v26, v25
	v_min_f32_e32 v20, 0x40e00000, v20
	v_cvt_pk_fp8_f32 v30, v24, v25 op_sel:[0,0,1]
	v_mul_f32_e32 v24, 0x3fd9db23, v20
	v_mul_f32_e32 v24, 0xbfb8aa3b, v24
	v_exp_f32_e32 v26, v24
	v_pk_fma_f32 v[22:23], v[22:23], s[20:21], v[242:243] op_sel_hi:[1,0,1]
	v_pk_fma_f32 v[16:17], v[16:17], s[20:21], v[244:245] op_sel_hi:[1,0,1]
	v_min_f32_e32 v22, 0x40e00000, v22
	v_add_f32_e32 v26, 1.0, v26
	v_mul_f32_e32 v27, 0x3fd9db23, v22
	v_rcp_f32_e32 v26, v26
	v_mul_f32_e32 v27, 0xbfb8aa3b, v27
	v_exp_f32_e32 v27, v27
	v_med3_f32 v21, v21, s61, v172
	v_mul_f32_e32 v20, v20, v26
	v_add_f32_e32 v21, 1.0, v21
	v_min_f32_e32 v16, 0x40e00000, v16
	v_add_f32_e32 v26, 1.0, v27
	v_mul_f32_e32 v20, v21, v20
	v_med3_f32 v21, v23, s61, v172
	v_mul_f32_e32 v23, 0x3fd9db23, v16
	v_rcp_f32_e32 v26, v26
	v_mul_f32_e32 v23, 0xbfb8aa3b, v23
	v_exp_f32_e32 v23, v23
	v_pk_fma_f32 v[18:19], v[18:19], s[20:21], v[246:247] op_sel_hi:[1,0,1]
	v_mul_f32_e32 v22, v22, v26
	v_add_f32_e32 v21, 1.0, v21
	v_min_f32_e32 v18, 0x40e00000, v18
	v_mul_f32_e32 v21, v21, v22
	v_add_f32_e32 v22, 1.0, v23
	v_mul_f32_e32 v23, 0x3fd9db23, v18
	v_rcp_f32_e32 v22, v22
	v_mul_f32_e32 v23, 0xbfb8aa3b, v23
	v_exp_f32_e32 v23, v23
	v_med3_f32 v17, v17, s61, v172
	v_mul_f32_e32 v16, v16, v22
	v_add_f32_e32 v17, 1.0, v17
	v_mul_f32_e32 v16, v17, v16
	v_add_f32_e32 v17, 1.0, v23
	v_rcp_f32_e32 v17, v17
	v_mov_b32_e32 v22, v145
	v_cvt_pk_fp8_f32 v22, v20, v21
	v_med3_f32 v19, v19, s61, v172
	v_mul_f32_e32 v17, v18, v17
	v_add_f32_e32 v18, 1.0, v19
	v_mul_f32_e32 v17, v18, v17
	v_cvt_pk_fp8_f32 v22, v16, v17 op_sel:[0,0,1]
	v_lshlrev_b64 v[32:33], 11, v[144:145]
	v_lshl_add_u64 v[32:33], s[16:17], 0, v[32:33]
	v_ashrrev_i32_e32 v149, 31, v148
	v_lshl_add_u64 v[24:25], v[32:33], 0, v[150:151]
	v_lshl_add_u64 v[16:17], v[32:33], 0, v[148:149]
	global_store_dword v[24:25], v30, off
	global_store_dword v[16:17], v22, off
.LBB0_1174:
	s_or_b64 exec, exec, s[10:11]
	v_add_u32_e32 v16, s39, v168
	v_cmp_gt_i32_e32 vcc, s38, v168
	s_nop 1
	v_cndmask_b32_e32 v144, -1, v16, vcc
	v_cmp_lt_i32_e32 vcc, -1, v144
	s_and_saveexec_b64 s[10:11], vcc
	s_cbranch_execz .LBB0_1176
	v_pk_fma_f32 v[12:13], v[12:13], s[20:21], v[232:233] op_sel_hi:[1,0,1]
	v_pk_fma_f32 v[14:15], v[14:15], s[20:21], v[234:235] op_sel_hi:[1,0,1]
	v_min_f32_e32 v12, 0x40e00000, v12
	v_mul_f32_e32 v18, 0x3fd9db23, v12
	v_mul_f32_e32 v18, 0xbfb8aa3b, v18
	v_exp_f32_e32 v18, v18
	v_min_f32_e32 v14, 0x40e00000, v14
	v_mul_f32_e32 v19, 0x3fd9db23, v14
	v_mul_f32_e32 v19, 0xbfb8aa3b, v19
	v_add_f32_e32 v18, 1.0, v18
	v_rcp_f32_e32 v18, v18
	v_exp_f32_e32 v19, v19
	v_pk_fma_f32 v[8:9], v[8:9], s[20:21], v[236:237] op_sel_hi:[1,0,1]
	v_med3_f32 v13, v13, s61, v172
	v_mul_f32_e32 v12, v12, v18
	v_add_f32_e32 v13, 1.0, v13
	v_min_f32_e32 v8, 0x40e00000, v8
	v_add_f32_e32 v18, 1.0, v19
	v_mul_f32_e32 v12, v13, v12
	v_med3_f32 v13, v15, s61, v172
	v_mul_f32_e32 v15, 0x3fd9db23, v8
	v_rcp_f32_e32 v18, v18
	v_mul_f32_e32 v15, 0xbfb8aa3b, v15
	v_exp_f32_e32 v15, v15
	v_pk_fma_f32 v[10:11], v[10:11], s[20:21], v[238:239] op_sel_hi:[1,0,1]
	v_mul_f32_e32 v14, v14, v18
	v_add_f32_e32 v13, 1.0, v13
	v_min_f32_e32 v10, 0x40e00000, v10
	v_mul_f32_e32 v13, v13, v14
	v_add_f32_e32 v14, 1.0, v15
	v_mul_f32_e32 v15, 0x3fd9db23, v10
	v_rcp_f32_e32 v14, v14
	v_mul_f32_e32 v15, 0xbfb8aa3b, v15
	v_exp_f32_e32 v15, v15
	v_med3_f32 v9, v9, s61, v172
	v_mul_f32_e32 v8, v8, v14
	v_add_f32_e32 v9, 1.0, v9
	v_mul_f32_e32 v8, v9, v8
	v_add_f32_e32 v9, 1.0, v15
	v_rcp_f32_e32 v9, v9
	v_mov_b32_e32 v14, v145
	v_cvt_pk_fp8_f32 v14, v12, v13
	v_med3_f32 v11, v11, s61, v172
	v_mul_f32_e32 v9, v10, v9
	v_add_f32_e32 v10, 1.0, v11
	v_pk_fma_f32 v[4:5], v[4:5], s[20:21], v[240:241] op_sel_hi:[1,0,1]
	v_mul_f32_e32 v9, v10, v9
	v_min_f32_e32 v4, 0x40e00000, v4
	v_cvt_pk_fp8_f32 v14, v8, v9 op_sel:[0,0,1]
	v_mul_f32_e32 v8, 0x3fd9db23, v4
	v_mul_f32_e32 v8, 0xbfb8aa3b, v8
	v_exp_f32_e32 v10, v8
	v_pk_fma_f32 v[6:7], v[6:7], s[20:21], v[242:243] op_sel_hi:[1,0,1]
	v_pk_fma_f32 v[0:1], v[0:1], s[20:21], v[244:245] op_sel_hi:[1,0,1]
	v_min_f32_e32 v6, 0x40e00000, v6
	v_add_f32_e32 v10, 1.0, v10
	v_mul_f32_e32 v11, 0x3fd9db23, v6
	v_rcp_f32_e32 v10, v10
	v_mul_f32_e32 v11, 0xbfb8aa3b, v11
	v_exp_f32_e32 v11, v11
	v_med3_f32 v5, v5, s61, v172
	v_mul_f32_e32 v4, v4, v10
	v_add_f32_e32 v5, 1.0, v5
	v_min_f32_e32 v0, 0x40e00000, v0
	v_add_f32_e32 v10, 1.0, v11
	v_mul_f32_e32 v4, v5, v4
	v_med3_f32 v5, v7, s61, v172
	v_mul_f32_e32 v7, 0x3fd9db23, v0
	v_rcp_f32_e32 v10, v10
	v_mul_f32_e32 v7, 0xbfb8aa3b, v7
	v_exp_f32_e32 v7, v7
	v_pk_fma_f32 v[2:3], v[2:3], s[20:21], v[246:247] op_sel_hi:[1,0,1]
	v_mul_f32_e32 v6, v6, v10
	v_add_f32_e32 v5, 1.0, v5
	v_min_f32_e32 v2, 0x40e00000, v2
	v_mul_f32_e32 v5, v5, v6
	v_add_f32_e32 v6, 1.0, v7
	v_mul_f32_e32 v7, 0x3fd9db23, v2
	v_rcp_f32_e32 v6, v6
	v_mul_f32_e32 v7, 0xbfb8aa3b, v7
	v_exp_f32_e32 v7, v7
	v_med3_f32 v1, v1, s61, v172
	v_mul_f32_e32 v0, v0, v6
	v_add_f32_e32 v1, 1.0, v1
	v_mul_f32_e32 v0, v1, v0
	v_add_f32_e32 v1, 1.0, v7
	v_rcp_f32_e32 v1, v1
	v_mov_b32_e32 v6, v145
	v_cvt_pk_fp8_f32 v6, v4, v5
	v_med3_f32 v3, v3, s61, v172
	v_mul_f32_e32 v1, v2, v1
	v_add_f32_e32 v2, 1.0, v3
	v_mul_f32_e32 v1, v2, v1
	v_cvt_pk_fp8_f32 v6, v0, v1 op_sel:[0,0,1]
	v_lshlrev_b64 v[16:17], 11, v[144:145]
	v_lshl_add_u64 v[16:17], s[16:17], 0, v[16:17]
	v_ashrrev_i32_e32 v149, 31, v148
	v_lshl_add_u64 v[8:9], v[16:17], 0, v[150:151]
	v_lshl_add_u64 v[0:1], v[16:17], 0, v[148:149]
	global_store_dword v[8:9], v14, off
	global_store_dword v[0:1], v6, off
